# v56 + nt on the two one-time streams: prologue f32 x row loads and the final pass's f32 output stores
# speedup vs baseline: 1.0081x; 1.0081x over previous
; __device__ __forceinline__ unsigned pk2(float lo, float hi) { unsigned r; asm("v_cvt_pk_bf16_f32 %0, %1, %2" : "=v"(r) : "v"(lo), "v"(hi)); return r; }
; __device__ __forceinline__ void first_norm_row(const float* xrow, const float* g, bf16* urow, bf16* hrow, int lane) {
;     const f32x4* xp = (const f32x4*)xrow; const f32x4* gp = (const f32x4*)g;
;     f32x4 v[4] = {xp[2 * lane], xp[2 * lane + 1], xp[128 + 2 * lane], xp[128 + 2 * lane + 1]};
;     float ss = 0.f;
; #pragma unroll
;     for (int i = 0; i < 4; ++i) ss += (v[i][0] * v[i][0] + v[i][1] * v[i][1]) + (v[i][2] * v[i][2] + v[i][3] * v[i][3]);
;     const float r = 1.0f / sqrtf(wave_sum(ss) * (1.0f / D) + RMS_EPS);
;     { v4u h0, h1; h0.x = pk2(v[0][0], v[0][1]); h0.y = pk2(v[0][2], v[0][3]); h0.z = pk2(v[1][0], v[1][1]); h0.w = pk2(v[1][2], v[1][3]);
;       h1.x = pk2(v[2][0], v[2][1]); h1.y = pk2(v[2][2], v[2][3]); h1.z = pk2(v[3][0], v[3][1]); h1.w = pk2(v[3][2], v[3][3]);
;       ((v4u*)hrow)[lane] = h0; ((v4u*)hrow)[64 + lane] = h1; }
;     const f32x4 g4[4] = {gp[2 * lane], gp[2 * lane + 1], gp[128 + 2 * lane], gp[128 + 2 * lane + 1]};
; #pragma unroll
;     for (int i = 0; i < 4; ++i) v[i] = v[i] * r * g4[i];
;     v4u o0, o1; o0.x = pk2(v[0][0], v[0][1]); o0.y = pk2(v[0][2], v[0][3]); o0.z = pk2(v[1][0], v[1][1]); o0.w = pk2(v[1][2], v[1][3]);
;     o1.x = pk2(v[2][0], v[2][1]); o1.y = pk2(v[2][2], v[2][3]); o1.z = pk2(v[3][0], v[3][1]); o1.w = pk2(v[3][2], v[3][3]);
;     ((v4u*)urow)[lane] = o0; ((v4u*)urow)[64 + lane] = o1;
.LBB0_91:
	s_waitcnt lgkmcnt(0)
	global_load_dwordx4 v[6:9], v[22:23], off nt
	global_load_dwordx4 v[2:5], v[22:23], off offset:16 nt
	global_load_dwordx4 v[10:13], v[22:23], off offset:2064 nt
	global_load_dwordx4 v[14:17], v[22:23], off offset:2048 nt
	v_lshl_add_u64 v[26:27], s[4:5], 0, v[20:21]
	v_add_co_u32_e32 v34, vcc, s11, v26
	s_add_i32 s9, s9, 1
	s_nop 0
	v_addc_co_u32_e32 v35, vcc, 0, v27, vcc
	v_lshl_add_u64 v[42:43], s[2:3], 0, v[20:21]
	s_add_u32 s2, s2, 0x800
	s_addc_u32 s3, s3, 0
	s_add_u32 s4, s4, 0x800
	s_addc_u32 s5, s5, 0
	v_lshl_add_u64 v[22:23], v[22:23], 0, s[6:7]
	s_cmp_ge_i32 s9, s8
	s_waitcnt vmcnt(0)
	v_cvt_pk_bf16_f32 v26, v6, v7
	v_cvt_pk_bf16_f32 v27, v8, v9
	v_cvt_pk_bf16_f32 v28, v2, v3
	v_cvt_pk_bf16_f32 v29, v4, v5
	v_pk_mul_f32 v[36:37], v[8:9], v[8:9]
	v_pk_mul_f32 v[44:45], v[6:7], v[6:7]
	v_pk_mul_f32 v[38:39], v[4:5], v[4:5]
	v_pk_mul_f32 v[46:47], v[2:3], v[2:3]
	v_mul_f32_e32 v40, v15, v15
	v_cvt_pk_bf16_f32 v30, v14, v15
	v_cvt_pk_bf16_f32 v31, v16, v17
	v_cvt_pk_bf16_f32 v32, v10, v11
	v_cvt_pk_bf16_f32 v33, v12, v13
	global_store_dwordx4 v[34:35], v[26:29], off sc1
	global_store_dwordx4 v[34:35], v[30:33], off offset:1024 sc1
	v_pk_mov_b32 v[50:51], v[44:45], v[36:37] op_sel:[1,0]
	v_mov_b32_e32 v45, v37
	v_pk_mov_b32 v[52:53], v[46:47], v[38:39] op_sel:[1,0]
	v_mov_b32_e32 v47, v39
	v_pk_fma_f32 v[54:55], v[14:15], v[14:15], v[40:41] op_sel_hi:[1,1,0]
	global_load_dwordx4 v[26:29], v[18:19], off
	global_load_dwordx4 v[30:33], v[18:19], off offset:16
	global_load_dwordx4 v[34:37], v[18:19], off offset:2048
	global_load_dwordx4 v[38:41], v[18:19], off offset:2064
	v_mul_f32_e32 v48, v17, v17
	v_pk_add_f32 v[44:45], v[50:51], v[44:45]
	v_pk_add_f32 v[46:47], v[52:53], v[46:47]
	v_mul_f32_e32 v25, v10, v10
	v_mul_f32_e32 v56, v11, v11
	v_mul_f32_e32 v57, v12, v12
	v_mul_f32_e32 v58, v13, v13
	v_pk_fma_f32 v[48:49], v[16:17], v[16:17], v[48:49] op_sel_hi:[1,1,0]
	v_pk_add_f32 v[44:45], v[44:45], v[44:45] op_sel:[0,1] op_sel_hi:[1,0]
	v_pk_add_f32 v[46:47], v[46:47], v[46:47] op_sel:[0,1] op_sel_hi:[1,0]
	v_mov_b32_e32 v55, v57
	v_mov_b32_e32 v49, v58
	v_mov_b32_e32 v45, v25
	v_mov_b32_e32 v47, v56
	v_pk_add_f32 v[48:49], v[54:55], v[48:49]
	v_pk_add_f32 v[44:45], v[44:45], v[46:47]
	s_nop 0
	v_pk_add_f32 v[44:45], v[44:45], v[48:49]
	s_nop 0
	v_add_f32_e32 v25, v44, v45
	s_nop 1
	v_add_f32_dpp v25, v25, v25 quad_perm:[1,0,3,2] row_mask:0xf bank_mask:0xf bound_ctrl:1
	s_nop 1
	v_add_f32_dpp v25, v25, v25 quad_perm:[2,3,0,1] row_mask:0xf bank_mask:0xf bound_ctrl:1
	s_nop 1
	v_add_f32_dpp v25, v25, v25 row_half_mirror row_mask:0xf bank_mask:0xf bound_ctrl:1
	s_nop 1
	v_add_f32_dpp v25, v25, v25 row_mirror row_mask:0xf bank_mask:0xf bound_ctrl:1
	s_nop 0
	v_readlane_b32 s13, v25, 16
	v_readlane_b32 s14, v25, 48
	v_readlane_b32 s0, v25, 0
	v_readlane_b32 s1, v25, 32
	v_mov_b32_e32 v44, s13
	v_mov_b32_e32 v45, s14
	v_pk_add_f32 v[44:45], s[0:1], v[44:45]
	s_nop 0
	v_add_f32_e32 v25, v44, v45
	v_fmamk_f32 v25, v25, 0x3a800000, v1
	v_mul_f32_e32 v44, 0x4f800000, v25
	v_cmp_gt_f32_e32 vcc, s10, v25
	s_nop 1
	v_cndmask_b32_e32 v25, v25, v44, vcc
	v_sqrt_f32_e32 v44, v25
	s_nop 0
	v_add_u32_e32 v45, -1, v44
	v_add_u32_e32 v46, 1, v44
	v_fma_f32 v47, -v45, v44, v25
	v_fma_f32 v48, -v46, v44, v25
	v_cmp_ge_f32_e64 s[0:1], 0, v47
	s_nop 1
	v_cndmask_b32_e64 v44, v44, v45, s[0:1]
	v_cmp_lt_f32_e64 s[0:1], 0, v48
	s_nop 1
	v_cndmask_b32_e64 v44, v44, v46, s[0:1]
	v_mul_f32_e32 v45, 0x37800000, v44
	v_cndmask_b32_e32 v44, v44, v45, vcc
	v_cmp_class_f32_e32 vcc, v25, v24
	s_nop 1
	v_cndmask_b32_e32 v25, v44, v25, vcc
	v_div_scale_f32 v44, s[0:1], v25, v25, 1.0
	v_rcp_f32_e32 v46, v44
	v_div_scale_f32 v45, vcc, 1.0, v25, 1.0
	v_fma_f32 v47, -v44, v46, 1.0
	v_fmac_f32_e32 v46, v47, v46
	v_mul_f32_e32 v47, v45, v46
	v_fma_f32 v48, -v44, v47, v45
	v_fmac_f32_e32 v47, v48, v46
	v_fma_f32 v44, -v44, v47, v45
	v_div_fmas_f32 v44, v44, v46, v47
	v_div_fixup_f32 v44, v44, v25, 1.0
	v_pk_mul_f32 v[6:7], v[6:7], v[44:45] op_sel_hi:[1,0]
	v_pk_mul_f32 v[2:3], v[2:3], v[44:45] op_sel_hi:[1,0]
	v_pk_mul_f32 v[4:5], v[4:5], v[44:45] op_sel_hi:[1,0]
	v_add_co_u32_e32 v42, vcc, s12, v42
	v_pk_mul_f32 v[8:9], v[8:9], v[44:45] op_sel_hi:[1,0]
	s_waitcnt vmcnt(3)
	v_pk_mul_f32 v[6:7], v[6:7], v[26:27]
	s_waitcnt vmcnt(2)
	v_pk_mul_f32 v[26:27], v[4:5], v[32:33]
	v_pk_mul_f32 v[4:5], v[2:3], v[30:31]
	v_addc_co_u32_e32 v43, vcc, 0, v43, vcc
	v_pk_mul_f32 v[14:15], v[14:15], v[44:45] op_sel_hi:[1,0]
	v_pk_mul_f32 v[16:17], v[16:17], v[44:45] op_sel_hi:[1,0]
	v_pk_mul_f32 v[10:11], v[10:11], v[44:45] op_sel_hi:[1,0]
	v_pk_mul_f32 v[12:13], v[12:13], v[44:45] op_sel_hi:[1,0]
	v_pk_mul_f32 v[8:9], v[8:9], v[28:29]
	v_cvt_pk_bf16_f32 v2, v6, v7
	v_cvt_pk_bf16_f32 v4, v4, v5
	v_cvt_pk_bf16_f32 v5, v26, v27
	s_waitcnt vmcnt(1)
	v_pk_mul_f32 v[16:17], v[16:17], v[36:37]
	v_cvt_pk_bf16_f32 v3, v8, v9
	v_pk_mul_f32 v[14:15], v[14:15], v[34:35]
	s_waitcnt vmcnt(0)
	v_pk_mul_f32 v[12:13], v[12:13], v[40:41]
	v_pk_mul_f32 v[10:11], v[10:11], v[38:39]
	v_cvt_pk_bf16_f32 v6, v14, v15
	v_cvt_pk_bf16_f32 v7, v16, v17
	v_cvt_pk_bf16_f32 v9, v12, v13
	s_nop 0
	v_cvt_pk_bf16_f32 v8, v10, v11
	flat_store_dwordx4 v[42:43], v[2:5] sc1
	flat_store_dwordx4 v[42:43], v[6:9] offset:1024 sc1
	s_cbranch_scc0 .LBB0_91
